# v28: v21 + code placement: the 12 GEMM K-loop heads aligned to 64 B, MLA loop head pinned at its baseline phase
# baseline (speedup 1.0000x reference)
.LBB0_243:
	s_add_u32 s0, s40, 0x100
	v_mov_b32_e32 v2, 0
	s_addc_u32 s1, s41, 0
	s_mov_b32 s3, -2
	v_mov_b32_e32 v3, v2
	v_mov_b32_e32 v4, v2
	v_mov_b32_e32 v5, v2
	v_mov_b32_e32 v6, v2
	v_mov_b32_e32 v7, v2
	v_mov_b32_e32 v8, v2
	v_mov_b32_e32 v9, v2
	v_mov_b32_e32 v18, v2
	v_mov_b32_e32 v19, v2
	v_mov_b32_e32 v20, v2
	v_mov_b32_e32 v21, v2
	v_mov_b32_e32 v22, v2
	v_mov_b32_e32 v23, v2
	v_mov_b32_e32 v24, v2
	v_mov_b32_e32 v25, v2
	s_waitcnt vmcnt(0)
	v_mov_b32_e32 v34, v2
	v_mov_b32_e32 v35, v2
	v_mov_b32_e32 v36, v2
	v_mov_b32_e32 v37, v2
	v_mov_b32_e32 v38, v2
	v_mov_b32_e32 v39, v2
	v_mov_b32_e32 v40, v2
	v_mov_b32_e32 v41, v2
	v_mov_b32_e32 v50, v2
	v_mov_b32_e32 v51, v2
	v_mov_b32_e32 v52, v2
	v_mov_b32_e32 v53, v2
	v_mov_b32_e32 v54, v2
	v_mov_b32_e32 v55, v2
	v_mov_b32_e32 v56, v2
	v_mov_b32_e32 v57, v2
	v_mov_b32_e32 v82, v2
	v_mov_b32_e32 v83, v2
	v_mov_b32_e32 v84, v2
	v_mov_b32_e32 v85, v2
	v_mov_b32_e32 v86, v2
	v_mov_b32_e32 v87, v2
	v_mov_b32_e32 v88, v2
	v_mov_b32_e32 v89, v2
	v_mov_b32_e32 v102, v2
	v_mov_b32_e32 v103, v2
	v_mov_b32_e32 v104, v2
	v_mov_b32_e32 v105, v2
	v_mov_b32_e32 v106, v2
	v_mov_b32_e32 v107, v2
	v_mov_b32_e32 v108, v2
	v_mov_b32_e32 v109, v2
	v_mov_b32_e32 v122, v2
	v_mov_b32_e32 v123, v2
	v_mov_b32_e32 v124, v2
	v_mov_b32_e32 v125, v2
	v_mov_b32_e32 v126, v2
	v_mov_b32_e32 v127, v2
	v_mov_b32_e32 v128, v2
	v_mov_b32_e32 v129, v2
	v_mov_b32_e32 v150, v2
	v_mov_b32_e32 v151, v2
	v_mov_b32_e32 v152, v2
	v_mov_b32_e32 v153, v2
	v_mov_b32_e32 v154, v2
	v_mov_b32_e32 v155, v2
	v_mov_b32_e32 v156, v2
	v_mov_b32_e32 v157, v2
	v_mov_b32_e32 v90, v2
	v_mov_b32_e32 v91, v2
	v_mov_b32_e32 v92, v2
	v_mov_b32_e32 v93, v2
	v_mov_b32_e32 v94, v2
	v_mov_b32_e32 v95, v2
	v_mov_b32_e32 v96, v2
	v_mov_b32_e32 v97, v2
	v_mov_b32_e32 v110, v2
	v_mov_b32_e32 v111, v2
	v_mov_b32_e32 v112, v2
	v_mov_b32_e32 v113, v2
	v_mov_b32_e32 v114, v2
	v_mov_b32_e32 v115, v2
	v_mov_b32_e32 v116, v2
	v_mov_b32_e32 v117, v2
	v_mov_b32_e32 v130, v2
	v_mov_b32_e32 v131, v2
	v_mov_b32_e32 v132, v2
	v_mov_b32_e32 v133, v2
	v_mov_b32_e32 v134, v2
	v_mov_b32_e32 v135, v2
	v_mov_b32_e32 v136, v2
	v_mov_b32_e32 v137, v2
	v_mov_b32_e32 v158, v2
	v_mov_b32_e32 v159, v2
	v_mov_b32_e32 v160, v2
	v_mov_b32_e32 v161, v2
	v_mov_b32_e32 v162, v2
	v_mov_b32_e32 v163, v2
	v_mov_b32_e32 v164, v2
	v_mov_b32_e32 v165, v2
	v_mov_b32_e32 v58, v2
	v_mov_b32_e32 v59, v2
	v_mov_b32_e32 v60, v2
	v_mov_b32_e32 v61, v2
	v_mov_b32_e32 v62, v2
	v_mov_b32_e32 v63, v2
	v_mov_b32_e32 v64, v2
	v_mov_b32_e32 v65, v2
	v_mov_b32_e32 v42, v2
	v_mov_b32_e32 v43, v2
	v_mov_b32_e32 v44, v2
	v_mov_b32_e32 v45, v2
	v_mov_b32_e32 v46, v2
	v_mov_b32_e32 v47, v2
	v_mov_b32_e32 v48, v2
	v_mov_b32_e32 v49, v2
	v_mov_b32_e32 v26, v2
	v_mov_b32_e32 v27, v2
	v_mov_b32_e32 v28, v2
	v_mov_b32_e32 v29, v2
	v_mov_b32_e32 v30, v2
	v_mov_b32_e32 v31, v2
	v_mov_b32_e32 v32, v2
	v_mov_b32_e32 v33, v2
	v_mov_b32_e32 v10, v2
	v_mov_b32_e32 v11, v2
	v_mov_b32_e32 v12, v2
	v_mov_b32_e32 v13, v2
	v_mov_b32_e32 v14, v2
	v_mov_b32_e32 v15, v2
	s_waitcnt lgkmcnt(0)
	v_mov_b32_e32 v16, v2
	v_mov_b32_e32 v17, v2
	.p2align	6

.LBB0_450:
	s_add_u32 s5, s46, 0x100
	s_addc_u32 s16, s47, 0
	s_add_u32 s17, s2, 0x100
	s_addc_u32 s18, s3, 0
	s_add_u32 s2, s2, 0x80
	s_addc_u32 s3, s3, 0
	s_mov_b32 s19, -2
	.p2align	6

.LBB0_563:
	s_add_u32 s0, s22, 0x100
	v_mov_b32_e32 v2, 0
	s_addc_u32 s1, s23, 0
	s_mov_b32 s13, -2
	s_waitcnt lgkmcnt(0)
	v_mov_b32_e32 v3, v2
	v_mov_b32_e32 v4, v2
	v_mov_b32_e32 v5, v2
	v_mov_b32_e32 v6, v2
	v_mov_b32_e32 v7, v2
	v_mov_b32_e32 v8, v2
	v_mov_b32_e32 v9, v2
	v_mov_b32_e32 v18, v2
	v_mov_b32_e32 v19, v2
	v_mov_b32_e32 v20, v2
	v_mov_b32_e32 v21, v2
	v_mov_b32_e32 v22, v2
	v_mov_b32_e32 v23, v2
	v_mov_b32_e32 v24, v2
	v_mov_b32_e32 v25, v2
	v_mov_b32_e32 v50, v2
	v_mov_b32_e32 v51, v2
	v_mov_b32_e32 v52, v2
	v_mov_b32_e32 v53, v2
	v_mov_b32_e32 v54, v2
	v_mov_b32_e32 v55, v2
	v_mov_b32_e32 v56, v2
	v_mov_b32_e32 v57, v2
	v_mov_b32_e32 v82, v2
	v_mov_b32_e32 v83, v2
	v_mov_b32_e32 v84, v2
	v_mov_b32_e32 v85, v2
	s_waitcnt vmcnt(1)
	v_mov_b32_e32 v86, v2
	v_mov_b32_e32 v87, v2
	v_mov_b32_e32 v88, v2
	v_mov_b32_e32 v89, v2
	v_mov_b32_e32 v98, v2
	v_mov_b32_e32 v99, v2
	v_mov_b32_e32 v100, v2
	v_mov_b32_e32 v101, v2
	v_mov_b32_e32 v102, v2
	v_mov_b32_e32 v103, v2
	v_mov_b32_e32 v104, v2
	v_mov_b32_e32 v105, v2
	v_mov_b32_e32 v114, v2
	v_mov_b32_e32 v115, v2
	v_mov_b32_e32 v116, v2
	v_mov_b32_e32 v117, v2
	v_mov_b32_e32 v118, v2
	v_mov_b32_e32 v119, v2
	v_mov_b32_e32 v120, v2
	v_mov_b32_e32 v121, v2
	v_mov_b32_e32 v130, v2
	v_mov_b32_e32 v131, v2
	v_mov_b32_e32 v132, v2
	v_mov_b32_e32 v133, v2
	s_waitcnt vmcnt(0)
	v_mov_b32_e32 v134, v2
	v_mov_b32_e32 v135, v2
	v_mov_b32_e32 v136, v2
	v_mov_b32_e32 v137, v2
	v_mov_b32_e32 v146, v2
	v_mov_b32_e32 v147, v2
	v_mov_b32_e32 v148, v2
	v_mov_b32_e32 v149, v2
	v_mov_b32_e32 v150, v2
	v_mov_b32_e32 v151, v2
	v_mov_b32_e32 v152, v2
	v_mov_b32_e32 v153, v2
	v_mov_b32_e32 v106, v2
	v_mov_b32_e32 v107, v2
	v_mov_b32_e32 v108, v2
	v_mov_b32_e32 v109, v2
	v_mov_b32_e32 v110, v2
	v_mov_b32_e32 v111, v2
	v_mov_b32_e32 v112, v2
	v_mov_b32_e32 v113, v2
	v_mov_b32_e32 v122, v2
	v_mov_b32_e32 v123, v2
	v_mov_b32_e32 v124, v2
	v_mov_b32_e32 v125, v2
	v_mov_b32_e32 v126, v2
	v_mov_b32_e32 v127, v2
	v_mov_b32_e32 v128, v2
	v_mov_b32_e32 v129, v2
	v_mov_b32_e32 v138, v2
	v_mov_b32_e32 v139, v2
	v_mov_b32_e32 v140, v2
	v_mov_b32_e32 v141, v2
	v_mov_b32_e32 v142, v2
	v_mov_b32_e32 v143, v2
	v_mov_b32_e32 v144, v2
	v_mov_b32_e32 v145, v2
	v_mov_b32_e32 v154, v2
	v_mov_b32_e32 v155, v2
	v_mov_b32_e32 v156, v2
	v_mov_b32_e32 v157, v2
	v_mov_b32_e32 v158, v2
	v_mov_b32_e32 v159, v2
	v_mov_b32_e32 v160, v2
	v_mov_b32_e32 v161, v2
	v_mov_b32_e32 v90, v2
	v_mov_b32_e32 v91, v2
	v_mov_b32_e32 v92, v2
	v_mov_b32_e32 v93, v2
	v_mov_b32_e32 v94, v2
	v_mov_b32_e32 v95, v2
	v_mov_b32_e32 v96, v2
	v_mov_b32_e32 v97, v2
	v_mov_b32_e32 v58, v2
	v_mov_b32_e32 v59, v2
	v_mov_b32_e32 v60, v2
	v_mov_b32_e32 v61, v2
	v_mov_b32_e32 v62, v2
	v_mov_b32_e32 v63, v2
	v_mov_b32_e32 v64, v2
	v_mov_b32_e32 v65, v2
	v_mov_b32_e32 v26, v2
	v_mov_b32_e32 v27, v2
	v_mov_b32_e32 v28, v2
	v_mov_b32_e32 v29, v2
	v_mov_b32_e32 v30, v2
	v_mov_b32_e32 v31, v2
	v_mov_b32_e32 v32, v2
	v_mov_b32_e32 v33, v2
	v_mov_b32_e32 v10, v2
	v_mov_b32_e32 v11, v2
	v_mov_b32_e32 v12, v2
	v_mov_b32_e32 v13, v2
	v_mov_b32_e32 v14, v2
	v_mov_b32_e32 v15, v2
	s_waitcnt lgkmcnt(0)
	v_mov_b32_e32 v16, v2
	v_mov_b32_e32 v17, v2
	.p2align	6

.LBB0_792:
	s_add_u32 s0, s22, 0x100
	v_mov_b32_e32 v2, 0
	s_addc_u32 s1, s23, 0
	s_mov_b32 s5, -2
	v_mov_b32_e32 v3, v2
	v_mov_b32_e32 v4, v2
	v_mov_b32_e32 v5, v2
	v_mov_b32_e32 v6, v2
	v_mov_b32_e32 v7, v2
	v_mov_b32_e32 v8, v2
	v_mov_b32_e32 v9, v2
	v_mov_b32_e32 v18, v2
	v_mov_b32_e32 v19, v2
	v_mov_b32_e32 v20, v2
	v_mov_b32_e32 v21, v2
	v_mov_b32_e32 v22, v2
	v_mov_b32_e32 v23, v2
	v_mov_b32_e32 v24, v2
	v_mov_b32_e32 v25, v2
	s_waitcnt vmcnt(0)
	v_mov_b32_e32 v34, v2
	v_mov_b32_e32 v35, v2
	v_mov_b32_e32 v36, v2
	v_mov_b32_e32 v37, v2
	v_mov_b32_e32 v38, v2
	v_mov_b32_e32 v39, v2
	v_mov_b32_e32 v40, v2
	v_mov_b32_e32 v41, v2
	v_mov_b32_e32 v50, v2
	v_mov_b32_e32 v51, v2
	v_mov_b32_e32 v52, v2
	v_mov_b32_e32 v53, v2
	v_mov_b32_e32 v54, v2
	v_mov_b32_e32 v55, v2
	v_mov_b32_e32 v56, v2
	v_mov_b32_e32 v57, v2
	v_mov_b32_e32 v66, v2
	v_mov_b32_e32 v67, v2
	v_mov_b32_e32 v68, v2
	v_mov_b32_e32 v69, v2
	v_mov_b32_e32 v70, v2
	v_mov_b32_e32 v71, v2
	v_mov_b32_e32 v72, v2
	v_mov_b32_e32 v73, v2
	v_mov_b32_e32 v106, v2
	v_mov_b32_e32 v107, v2
	v_mov_b32_e32 v108, v2
	v_mov_b32_e32 v109, v2
	v_mov_b32_e32 v114, v2
	v_mov_b32_e32 v115, v2
	v_mov_b32_e32 v116, v2
	v_mov_b32_e32 v117, v2
	v_mov_b32_e32 v146, v2
	v_mov_b32_e32 v147, v2
	v_mov_b32_e32 v148, v2
	v_mov_b32_e32 v149, v2
	v_mov_b32_e32 v150, v2
	v_mov_b32_e32 v151, v2
	v_mov_b32_e32 v152, v2
	v_mov_b32_e32 v153, v2
	v_mov_b32_e32 v178, v2
	v_mov_b32_e32 v179, v2
	v_mov_b32_e32 v180, v2
	v_mov_b32_e32 v181, v2
	v_mov_b32_e32 v182, v2
	v_mov_b32_e32 v183, v2
	v_mov_b32_e32 v184, v2
	v_mov_b32_e32 v185, v2
	v_mov_b32_e32 v78, v2
	v_mov_b32_e32 v79, v2
	v_mov_b32_e32 v80, v2
	v_mov_b32_e32 v81, v2
	v_mov_b32_e32 v82, v2
	v_mov_b32_e32 v83, v2
	v_mov_b32_e32 v84, v2
	v_mov_b32_e32 v85, v2
	v_mov_b32_e32 v122, v2
	v_mov_b32_e32 v123, v2
	v_mov_b32_e32 v124, v2
	v_mov_b32_e32 v125, v2
	v_mov_b32_e32 v126, v2
	v_mov_b32_e32 v127, v2
	v_mov_b32_e32 v128, v2
	v_mov_b32_e32 v129, v2
	v_mov_b32_e32 v154, v2
	v_mov_b32_e32 v155, v2
	v_mov_b32_e32 v156, v2
	v_mov_b32_e32 v157, v2
	v_mov_b32_e32 v158, v2
	v_mov_b32_e32 v159, v2
	v_mov_b32_e32 v160, v2
	v_mov_b32_e32 v161, v2
	v_mov_b32_e32 v186, v2
	v_mov_b32_e32 v187, v2
	v_mov_b32_e32 v188, v2
	v_mov_b32_e32 v189, v2
	v_mov_b32_e32 v190, v2
	v_mov_b32_e32 v191, v2
	v_mov_b32_e32 v192, v2
	v_mov_b32_e32 v193, v2
	v_mov_b32_e32 v58, v2
	v_mov_b32_e32 v59, v2
	v_mov_b32_e32 v60, v2
	v_mov_b32_e32 v61, v2
	v_mov_b32_e32 v62, v2
	v_mov_b32_e32 v63, v2
	v_mov_b32_e32 v64, v2
	v_mov_b32_e32 v65, v2
	v_mov_b32_e32 v42, v2
	v_mov_b32_e32 v43, v2
	v_mov_b32_e32 v44, v2
	v_mov_b32_e32 v45, v2
	v_mov_b32_e32 v46, v2
	v_mov_b32_e32 v47, v2
	v_mov_b32_e32 v48, v2
	v_mov_b32_e32 v49, v2
	v_mov_b32_e32 v26, v2
	v_mov_b32_e32 v27, v2
	v_mov_b32_e32 v28, v2
	v_mov_b32_e32 v29, v2
	v_mov_b32_e32 v30, v2
	v_mov_b32_e32 v31, v2
	v_mov_b32_e32 v32, v2
	v_mov_b32_e32 v33, v2
	v_mov_b32_e32 v10, v2
	v_mov_b32_e32 v11, v2
	v_mov_b32_e32 v12, v2
	v_mov_b32_e32 v13, v2
	v_mov_b32_e32 v14, v2
	v_mov_b32_e32 v15, v2
	v_mov_b32_e32 v16, v2
	v_mov_b32_e32 v17, v2
	.p2align	6

.LBB0_856:
	s_waitcnt vmcnt(7)
	v_mov_b32_e32 v66, 0
	s_mov_b64 s[50:51], 0
	s_mov_b64 s[46:47], -1
	s_mov_b64 s[48:49], 0
	v_mov_b32_e32 v67, v66
	v_mov_b32_e32 v68, v66
	v_mov_b32_e32 v69, v66
	s_waitcnt vmcnt(4)
	v_mov_b32_e32 v70, v66
	v_mov_b32_e32 v71, v66
	v_mov_b32_e32 v72, v66
	v_mov_b32_e32 v73, v66
	v_mov_b32_e32 v82, v66
	v_mov_b32_e32 v83, v66
	v_mov_b32_e32 v84, v66
	v_mov_b32_e32 v85, v66
	s_waitcnt vmcnt(1)
	v_mov_b32_e32 v86, v66
	v_mov_b32_e32 v87, v66
	v_mov_b32_e32 v88, v66
	v_mov_b32_e32 v89, v66
	v_mov_b32_e32 v98, v66
	v_mov_b32_e32 v99, v66
	v_mov_b32_e32 v100, v66
	v_mov_b32_e32 v101, v66
	v_mov_b32_e32 v102, v66
	v_mov_b32_e32 v103, v66
	v_mov_b32_e32 v104, v66
	v_mov_b32_e32 v105, v66
	v_mov_b32_e32 v114, v66
	v_mov_b32_e32 v115, v66
	v_mov_b32_e32 v116, v66
	v_mov_b32_e32 v117, v66
	v_mov_b32_e32 v118, v66
	v_mov_b32_e32 v119, v66
	v_mov_b32_e32 v120, v66
	v_mov_b32_e32 v121, v66
	v_mov_b32_e32 v130, v66
	v_mov_b32_e32 v131, v66
	v_mov_b32_e32 v132, v66
	v_mov_b32_e32 v133, v66
	s_waitcnt vmcnt(0)
	v_mov_b32_e32 v134, v66
	v_mov_b32_e32 v135, v66
	v_mov_b32_e32 v136, v66
	v_mov_b32_e32 v137, v66
	v_mov_b32_e32 v146, v66
	v_mov_b32_e32 v147, v66
	v_mov_b32_e32 v148, v66
	v_mov_b32_e32 v149, v66
	v_mov_b32_e32 v150, v66
	v_mov_b32_e32 v151, v66
	v_mov_b32_e32 v152, v66
	v_mov_b32_e32 v153, v66
	v_mov_b32_e32 v162, v66
	v_mov_b32_e32 v163, v66
	v_mov_b32_e32 v164, v66
	v_mov_b32_e32 v165, v66
	v_mov_b32_e32 v166, v66
	v_mov_b32_e32 v167, v66
	v_mov_b32_e32 v168, v66
	v_mov_b32_e32 v169, v66
	v_mov_b32_e32 v178, v66
	v_mov_b32_e32 v179, v66
	v_mov_b32_e32 v180, v66
	v_mov_b32_e32 v181, v66
	v_mov_b32_e32 v182, v66
	v_mov_b32_e32 v183, v66
	v_mov_b32_e32 v184, v66
	v_mov_b32_e32 v185, v66
	v_mov_b32_e32 v138, v66
	v_mov_b32_e32 v139, v66
	v_mov_b32_e32 v140, v66
	v_mov_b32_e32 v141, v66
	v_mov_b32_e32 v142, v66
	v_mov_b32_e32 v143, v66
	v_mov_b32_e32 v144, v66
	v_mov_b32_e32 v145, v66
	v_mov_b32_e32 v154, v66
	v_mov_b32_e32 v155, v66
	v_mov_b32_e32 v156, v66
	v_mov_b32_e32 v157, v66
	v_mov_b32_e32 v158, v66
	v_mov_b32_e32 v159, v66
	v_mov_b32_e32 v160, v66
	v_mov_b32_e32 v161, v66
	v_mov_b32_e32 v170, v66
	v_mov_b32_e32 v171, v66
	v_mov_b32_e32 v172, v66
	v_mov_b32_e32 v173, v66
	v_mov_b32_e32 v174, v66
	v_mov_b32_e32 v175, v66
	v_mov_b32_e32 v176, v66
	v_mov_b32_e32 v177, v66
	v_mov_b32_e32 v186, v66
	v_mov_b32_e32 v187, v66
	v_mov_b32_e32 v188, v66
	v_mov_b32_e32 v189, v66
	v_mov_b32_e32 v190, v66
	v_mov_b32_e32 v191, v66
	v_mov_b32_e32 v192, v66
	v_mov_b32_e32 v193, v66
	v_mov_b32_e32 v122, v66
	v_mov_b32_e32 v123, v66
	v_mov_b32_e32 v124, v66
	v_mov_b32_e32 v125, v66
	v_mov_b32_e32 v126, v66
	v_mov_b32_e32 v127, v66
	v_mov_b32_e32 v128, v66
	v_mov_b32_e32 v129, v66
	v_mov_b32_e32 v106, v66
	v_mov_b32_e32 v107, v66
	v_mov_b32_e32 v108, v66
	v_mov_b32_e32 v109, v66
	v_mov_b32_e32 v110, v66
	v_mov_b32_e32 v111, v66
	v_mov_b32_e32 v112, v66
	v_mov_b32_e32 v113, v66
	s_waitcnt vmcnt(0)
	v_mov_b32_e32 v90, v66
	v_mov_b32_e32 v91, v66
	v_mov_b32_e32 v92, v66
	v_mov_b32_e32 v93, v66
	v_mov_b32_e32 v94, v66
	v_mov_b32_e32 v95, v66
	v_mov_b32_e32 v96, v66
	v_mov_b32_e32 v97, v66
	v_mov_b32_e32 v74, v66
	v_mov_b32_e32 v75, v66
	v_mov_b32_e32 v76, v66
	v_mov_b32_e32 v77, v66
	v_mov_b32_e32 v78, v66
	v_mov_b32_e32 v79, v66
	v_mov_b32_e32 v80, v66
	v_mov_b32_e32 v81, v66
	.p2align	6

.LBB0_941:
	v_and_b32_e32 v1, 63, v194
	v_lshlrev_b32_e32 v4, 4, v1
	v_lshlrev_b32_e32 v3, 3, v1
	v_and_b32_e32 v4, 0xc0, v4
	v_lshlrev_b32_e32 v5, 1, v1
	v_and_b32_e32 v2, 15, v194
	v_and_or_b32 v4, v3, 24, v4
	v_and_b32_e32 v5, 32, v5
	v_and_b32_e32 v3, 0x100, v3
	v_or3_b32 v19, v4, v5, v3
	v_lshlrev_b32_e32 v3, 8, v195
	v_xor_b32_e32 v2, v196, v2
	v_lshl_or_b32 v202, v2, 4, v3
	v_add_u32_e32 v30, 0, v202
	s_waitcnt vmcnt(0)
	s_waitcnt vmcnt(63) expcnt(7) lgkmcnt(15)
	s_barrier
	ds_read_b128 v[22:25], v30 offset:49152
	ds_read_b128 v[26:29], v30 offset:57344
	v_xor_b32_e32 v30, 0x80, v30
	v_and_b32_e32 v4, 0xf0, v21
	v_or_b32_e32 v2, 32, v20
	s_waitcnt vmcnt(11) lgkmcnt(1)
	v_mfma_f32_32x32x16_bf16 v[66:81], v[22:25], v[130:133], 0
	v_bitop3_b32 v207, v2, v3, v4 bitop3:0xde
	v_add_u32_e32 v31, 0, v207
	v_or_b32_e32 v2, 64, v20
	v_bitop3_b32 v209, v2, v3, v4 bitop3:0xde
	v_add_u32_e32 v32, 0, v209
	v_or_b32_e32 v2, 0x60, v20
	v_bitop3_b32 v224, v2, v3, v4 bitop3:0xde
	s_waitcnt lgkmcnt(0)
	v_mfma_f32_32x32x16_bf16 v[82:97], v[26:29], v[130:133], 0
	ds_read_b128 v[22:25], v31 offset:49152
	ds_read_b128 v[26:29], v31 offset:57344
	v_xor_b32_e32 v31, 0x80, v31
	v_add_u32_e32 v33, 0, v224
	s_xor_b64 s[66:67], s[2:3], -1
	s_add_i32 s2, s1, 0x100
	s_add_i32 s35, s35, s1
	s_add_i32 s1, 0, 0x18000
	v_lshl_add_u32 v225, v195, 7, s1
	s_waitcnt vmcnt(10) lgkmcnt(1)
	v_mfma_f32_32x32x16_bf16 v[66:81], v[22:25], v[134:137], v[66:81]
	s_movk_i32 s1, 0x70
	v_lshlrev_b32_e32 v4, 3, v194
	v_and_b32_e32 v4, 0x70, v4
	v_xor_b32_e32 v226, v20, v4
	v_bitop3_b32 v206, v20, v4, 32 bitop3:0x36
	v_bitop3_b32 v208, v20, v4, 64 bitop3:0x36
	v_bitop3_b32 v223, v20, v4, s94 bitop3:0x36
	s_and_b32 s0, s0, 0x3fffffc0
	s_lshl_b32 s0, s0, 2
	s_waitcnt lgkmcnt(0)
	v_mfma_f32_32x32x16_bf16 v[82:97], v[26:29], v[134:137], v[82:97]
	ds_read_b128 v[22:25], v32 offset:49152
	ds_read_b128 v[26:29], v32 offset:57344
	v_xor_b32_e32 v32, 0x80, v32
	s_add_i32 s0, s0, 0
	s_mov_b32 s40, 0
	s_add_i32 s0, s0, 0x1e000
	s_mov_b32 s41, s40
	s_lshr_b32 s21, s2, 6
	s_mov_b32 s42, s40
	s_waitcnt vmcnt(9) lgkmcnt(1)
	v_mfma_f32_32x32x16_bf16 v[66:81], v[22:25], v[138:141], v[66:81]
	s_mov_b32 s43, s40
	s_mov_b32 s44, s40
	s_mov_b32 s45, s40
	s_mov_b32 s46, s40
	s_mov_b32 s47, s40
	s_mov_b32 s48, s40
	s_mov_b32 s49, s40
	s_waitcnt lgkmcnt(0)
	v_mfma_f32_32x32x16_bf16 v[82:97], v[26:29], v[138:141], v[82:97]
	ds_read_b128 v[22:25], v33 offset:49152
	ds_read_b128 v[26:29], v33 offset:57344
	v_xor_b32_e32 v33, 0x80, v33
	s_mov_b32 s50, s40
	s_mov_b32 s51, s40
	s_mov_b32 s52, s40
	s_mov_b32 s53, s40
	s_mov_b32 s54, s40
	s_mov_b32 s55, s40
	s_waitcnt vmcnt(8) lgkmcnt(1)
	v_mfma_f32_32x32x16_bf16 v[66:81], v[22:25], v[142:145], v[66:81]
	v_mov_b64_e32 v[2:3], s[40:41]
	v_cmp_gt_u32_e64 s[2:3], 32, v1
	v_lshl_add_u32 v227, v195, 2, s0
	v_lshl_add_u32 v1, v196, 4, s0
	s_sub_i32 s0, s35, 27
	v_lshlrev_b32_e32 v18, 2, v196
	v_mov_b64_e32 v[16:17], s[54:55]
	s_waitcnt lgkmcnt(0)
	v_mfma_f32_32x32x16_bf16 v[82:97], v[26:29], v[142:145], v[82:97]
	ds_read_b128 v[22:25], v30 offset:49152
	ds_read_b128 v[26:29], v30 offset:57344
	v_add_u32_e32 v228, 0, v19
	v_add_u32_e32 v19, s0, v195
	v_mov_b64_e32 v[4:5], s[42:43]
	v_mov_b64_e32 v[6:7], s[44:45]
	v_mov_b64_e32 v[8:9], s[46:47]
	v_mov_b64_e32 v[10:11], s[48:49]
	s_waitcnt vmcnt(7) lgkmcnt(1)
	v_mfma_f32_32x32x16_bf16 v[66:81], v[22:25], v[146:149], v[66:81]
	v_mov_b64_e32 v[12:13], s[50:51]
	v_mov_b64_e32 v[14:15], s[52:53]
	v_sub_u32_e32 v229, v19, v18
	v_mov_b64_e32 v[48:49], v[16:17]
	v_mov_b64_e32 v[64:65], v[16:17]
	s_mov_b32 s34, 3
	v_mov_b32_e32 v230, 0
	s_waitcnt lgkmcnt(0)
	v_mfma_f32_32x32x16_bf16 v[82:97], v[26:29], v[146:149], v[82:97]
	ds_read_b128 v[22:25], v31 offset:49152
	ds_read_b128 v[26:29], v31 offset:57344
	v_mov_b32_e32 v231, 0xf149f2ca
	s_movk_i32 s37, 0x7f
	s_mov_b64 s[22:23], s[64:65]
	s_mov_b64 s[42:43], s[62:63]
	v_mov_b64_e32 v[46:47], v[14:15]
	v_mov_b64_e32 v[44:45], v[12:13]
	s_waitcnt vmcnt(6) lgkmcnt(1)
	v_mfma_f32_32x32x16_bf16 v[66:81], v[22:25], v[150:153], v[66:81]
	v_mov_b64_e32 v[42:43], v[10:11]
	v_mov_b64_e32 v[40:41], v[8:9]
	v_mov_b64_e32 v[38:39], v[6:7]
	v_mov_b64_e32 v[36:37], v[4:5]
	v_mov_b64_e32 v[34:35], v[2:3]
	v_mov_b64_e32 v[62:63], v[14:15]
	v_mov_b64_e32 v[60:61], v[12:13]
	s_waitcnt lgkmcnt(0)
	v_mfma_f32_32x32x16_bf16 v[82:97], v[26:29], v[150:153], v[82:97]
	ds_read_b128 v[22:25], v32 offset:49152
	ds_read_b128 v[26:29], v32 offset:57344
	v_mov_b64_e32 v[58:59], v[10:11]
	v_mov_b64_e32 v[56:57], v[8:9]
	v_mov_b64_e32 v[54:55], v[6:7]
	v_mov_b64_e32 v[52:53], v[4:5]
	v_mov_b64_e32 v[50:51], v[2:3]
	s_waitcnt vmcnt(5) lgkmcnt(1)
	v_mfma_f32_32x32x16_bf16 v[66:81], v[22:25], v[154:157], v[66:81]
	s_waitcnt lgkmcnt(0)
	v_mfma_f32_32x32x16_bf16 v[82:97], v[26:29], v[154:157], v[82:97]
	ds_read_b128 v[22:25], v33 offset:49152
	ds_read_b128 v[26:29], v33 offset:57344
	s_waitcnt vmcnt(4) lgkmcnt(1)
	v_mfma_f32_32x32x16_bf16 v[66:81], v[22:25], v[158:161], v[66:81]
	v_add_u32_e32 v24, v225, v226
	s_waitcnt lgkmcnt(0)
	v_mfma_f32_32x32x16_bf16 v[82:97], v[26:29], v[158:161], v[82:97]
	ds_read_b128 v[20:23], v24
	ds_read_b128 v[24:27], v24 offset:4096
	s_waitcnt vmcnt(3) lgkmcnt(1)
	v_mfma_f32_32x32x16_bf16 v[66:81], v[20:23], v[162:165], v[66:81]
	s_waitcnt lgkmcnt(0)
	v_mfma_f32_32x32x16_bf16 v[82:97], v[24:27], v[162:165], v[82:97]
	v_add_u32_e32 v24, v225, v206
	ds_read_b128 v[20:23], v24
	ds_read_b128 v[24:27], v24 offset:4096
	s_waitcnt vmcnt(2) lgkmcnt(1)
	v_mfma_f32_32x32x16_bf16 v[66:81], v[20:23], v[166:169], v[66:81]
	s_waitcnt lgkmcnt(0)
	v_mfma_f32_32x32x16_bf16 v[82:97], v[24:27], v[166:169], v[82:97]
	v_add_u32_e32 v24, v225, v208
	ds_read_b128 v[20:23], v24
	ds_read_b128 v[24:27], v24 offset:4096
	s_waitcnt vmcnt(1) lgkmcnt(1)
	v_mfma_f32_32x32x16_bf16 v[66:81], v[20:23], v[170:173], v[66:81]
	s_waitcnt lgkmcnt(0)
	v_mfma_f32_32x32x16_bf16 v[82:97], v[24:27], v[170:173], v[82:97]
	v_add_u32_e32 v24, v225, v223
	ds_read_b128 v[20:23], v24
	ds_read_b128 v[24:27], v24 offset:4096
	s_waitcnt vmcnt(0) lgkmcnt(1)
	v_mfma_f32_32x32x16_bf16 v[66:81], v[20:23], v[174:177], v[66:81]
	s_waitcnt lgkmcnt(0)
	v_mfma_f32_32x32x16_bf16 v[82:97], v[24:27], v[174:177], v[82:97]
	v_mov_b64_e32 v[32:33], v[16:17]
	v_mov_b64_e32 v[30:31], v[14:15]
	v_mov_b64_e32 v[28:29], v[12:13]
	v_mov_b64_e32 v[26:27], v[10:11]
	v_mov_b64_e32 v[24:25], v[8:9]
	v_mov_b64_e32 v[22:23], v[6:7]
	v_mov_b64_e32 v[20:21], v[4:5]
	v_mov_b64_e32 v[18:19], v[2:3]
	.p2align	6
	s_nop 0
	s_nop 0
	s_nop 0
	s_nop 0
	s_nop 0
	s_nop 0
	s_nop 0
	s_nop 0
	s_nop 0
	s_nop 0

.LBB0_1160:
	s_add_u32 s5, s44, 0x100
	s_addc_u32 s16, s45, 0
	s_add_u32 s17, s42, 0x100
	s_addc_u32 s18, s43, 0
	s_add_u32 s42, s42, 0x80
	s_addc_u32 s43, s43, 0
	s_mov_b32 s19, -2
	.p2align	6

.LBB0_1728:
	s_add_u32 s16, s22, 0x100
	s_addc_u32 s17, s23, 0
	s_mov_b32 s18, -2
	s_mov_b64 s[56:57], s[30:31]
	.p2align	6

.LBB0_1814:
	s_add_u32 s18, s22, 0x100
	s_addc_u32 s19, s23, 0
	s_mov_b32 s21, -2
	.p2align	6

.LBB0_1938:
	s_add_u32 s0, s22, 0x100
	v_mov_b32_e32 v2, 0
	s_addc_u32 s1, s23, 0
	s_mov_b32 s3, -2
	v_mov_b32_e32 v3, v2
	v_mov_b32_e32 v4, v2
	v_mov_b32_e32 v5, v2
	v_mov_b32_e32 v10, v2
	v_mov_b32_e32 v11, v2
	v_mov_b32_e32 v12, v2
	v_mov_b32_e32 v13, v2
	v_mov_b32_e32 v18, v2
	v_mov_b32_e32 v19, v2
	v_mov_b32_e32 v20, v2
	v_mov_b32_e32 v21, v2
	v_mov_b32_e32 v26, v2
	v_mov_b32_e32 v27, v2
	v_mov_b32_e32 v28, v2
	v_mov_b32_e32 v29, v2
	s_waitcnt vmcnt(0)
	v_mov_b32_e32 v34, v2
	v_mov_b32_e32 v35, v2
	v_mov_b32_e32 v36, v2
	v_mov_b32_e32 v37, v2
	v_mov_b32_e32 v42, v2
	v_mov_b32_e32 v43, v2
	v_mov_b32_e32 v44, v2
	v_mov_b32_e32 v45, v2
	v_mov_b32_e32 v54, v2
	v_mov_b32_e32 v55, v2
	v_mov_b32_e32 v56, v2
	v_mov_b32_e32 v57, v2
	v_mov_b32_e32 v62, v2
	v_mov_b32_e32 v63, v2
	v_mov_b32_e32 v64, v2
	v_mov_b32_e32 v65, v2
	v_mov_b32_e32 v74, v2
	v_mov_b32_e32 v75, v2
	v_mov_b32_e32 v76, v2
	v_mov_b32_e32 v77, v2
	v_mov_b32_e32 v82, v2
	v_mov_b32_e32 v83, v2
	v_mov_b32_e32 v84, v2
	v_mov_b32_e32 v85, v2
	v_mov_b32_e32 v94, v2
	v_mov_b32_e32 v95, v2
	v_mov_b32_e32 v96, v2
	v_mov_b32_e32 v97, v2
	v_mov_b32_e32 v102, v2
	v_mov_b32_e32 v103, v2
	v_mov_b32_e32 v104, v2
	v_mov_b32_e32 v105, v2
	v_mov_b32_e32 v114, v2
	v_mov_b32_e32 v115, v2
	v_mov_b32_e32 v116, v2
	v_mov_b32_e32 v117, v2
	v_mov_b32_e32 v122, v2
	v_mov_b32_e32 v123, v2
	v_mov_b32_e32 v124, v2
	v_mov_b32_e32 v125, v2
	v_mov_b32_e32 v138, v2
	v_mov_b32_e32 v139, v2
	v_mov_b32_e32 v140, v2
	v_mov_b32_e32 v141, v2
	v_mov_b32_e32 v146, v2
	v_mov_b32_e32 v147, v2
	v_mov_b32_e32 v148, v2
	v_mov_b32_e32 v149, v2
	v_mov_b32_e32 v78, v2
	v_mov_b32_e32 v79, v2
	v_mov_b32_e32 v80, v2
	v_mov_b32_e32 v81, v2
	v_mov_b32_e32 v86, v2
	v_mov_b32_e32 v87, v2
	v_mov_b32_e32 v88, v2
	v_mov_b32_e32 v89, v2
	v_mov_b32_e32 v98, v2
	v_mov_b32_e32 v99, v2
	v_mov_b32_e32 v100, v2
	v_mov_b32_e32 v101, v2
	v_mov_b32_e32 v106, v2
	v_mov_b32_e32 v107, v2
	v_mov_b32_e32 v108, v2
	v_mov_b32_e32 v109, v2
	v_mov_b32_e32 v118, v2
	v_mov_b32_e32 v119, v2
	v_mov_b32_e32 v120, v2
	v_mov_b32_e32 v121, v2
	v_mov_b32_e32 v126, v2
	v_mov_b32_e32 v127, v2
	v_mov_b32_e32 v128, v2
	v_mov_b32_e32 v129, v2
	v_mov_b32_e32 v142, v2
	v_mov_b32_e32 v143, v2
	v_mov_b32_e32 v144, v2
	v_mov_b32_e32 v145, v2
	v_mov_b32_e32 v150, v2
	v_mov_b32_e32 v151, v2
	v_mov_b32_e32 v152, v2
	v_mov_b32_e32 v153, v2
	v_mov_b32_e32 v66, v2
	v_mov_b32_e32 v67, v2
	v_mov_b32_e32 v68, v2
	v_mov_b32_e32 v69, v2
	v_mov_b32_e32 v58, v2
	v_mov_b32_e32 v59, v2
	v_mov_b32_e32 v60, v2
	v_mov_b32_e32 v61, v2
	v_mov_b32_e32 v46, v2
	v_mov_b32_e32 v47, v2
	v_mov_b32_e32 v48, v2
	v_mov_b32_e32 v49, v2
	v_mov_b32_e32 v38, v2
	v_mov_b32_e32 v39, v2
	v_mov_b32_e32 v40, v2
	v_mov_b32_e32 v41, v2
	v_mov_b32_e32 v30, v2
	v_mov_b32_e32 v31, v2
	v_mov_b32_e32 v32, v2
	v_mov_b32_e32 v33, v2
	v_mov_b32_e32 v22, v2
	v_mov_b32_e32 v23, v2
	v_mov_b32_e32 v24, v2
	v_mov_b32_e32 v25, v2
	v_mov_b32_e32 v14, v2
	v_mov_b32_e32 v15, v2
	v_mov_b32_e32 v16, v2
	v_mov_b32_e32 v17, v2
	v_mov_b32_e32 v6, v2
	v_mov_b32_e32 v7, v2
	v_mov_b32_e32 v8, v2
	v_mov_b32_e32 v9, v2
	.p2align	6

.LBB0_1958:
	s_add_u32 s5, s42, 0x100
	s_addc_u32 s13, s43, 0
	s_mov_b32 s17, -2
	.p2align	6

.LBB0_2034:
	s_add_u32 s0, s26, 0x100
	v_mov_b32_e32 v2, 0
	s_addc_u32 s1, s27, 0
	s_mov_b32 s5, -2
	s_waitcnt lgkmcnt(0)
	v_mov_b32_e32 v3, v2
	v_mov_b32_e32 v4, v2
	v_mov_b32_e32 v5, v2
	v_mov_b32_e32 v6, v2
	v_mov_b32_e32 v7, v2
	v_mov_b32_e32 v8, v2
	v_mov_b32_e32 v9, v2
	v_mov_b32_e32 v18, v2
	v_mov_b32_e32 v19, v2
	v_mov_b32_e32 v20, v2
	v_mov_b32_e32 v21, v2
	v_mov_b32_e32 v22, v2
	v_mov_b32_e32 v23, v2
	v_mov_b32_e32 v24, v2
	v_mov_b32_e32 v25, v2
	s_waitcnt vmcnt(0)
	v_mov_b32_e32 v34, v2
	v_mov_b32_e32 v35, v2
	v_mov_b32_e32 v36, v2
	v_mov_b32_e32 v37, v2
	v_mov_b32_e32 v38, v2
	v_mov_b32_e32 v39, v2
	v_mov_b32_e32 v40, v2
	v_mov_b32_e32 v41, v2
	v_mov_b32_e32 v50, v2
	v_mov_b32_e32 v51, v2
	v_mov_b32_e32 v52, v2
	v_mov_b32_e32 v53, v2
	v_mov_b32_e32 v54, v2
	v_mov_b32_e32 v55, v2
	v_mov_b32_e32 v56, v2
	v_mov_b32_e32 v57, v2
	v_mov_b32_e32 v66, v2
	v_mov_b32_e32 v67, v2
	v_mov_b32_e32 v68, v2
	v_mov_b32_e32 v69, v2
	v_mov_b32_e32 v70, v2
	v_mov_b32_e32 v71, v2
	v_mov_b32_e32 v72, v2
	v_mov_b32_e32 v73, v2
	v_mov_b32_e32 v82, v2
	v_mov_b32_e32 v83, v2
	v_mov_b32_e32 v84, v2
	v_mov_b32_e32 v85, v2
	v_mov_b32_e32 v86, v2
	v_mov_b32_e32 v87, v2
	v_mov_b32_e32 v88, v2
	v_mov_b32_e32 v89, v2
	v_mov_b32_e32 v98, v2
	v_mov_b32_e32 v99, v2
	v_mov_b32_e32 v100, v2
	v_mov_b32_e32 v101, v2
	v_mov_b32_e32 v102, v2
	v_mov_b32_e32 v103, v2
	v_mov_b32_e32 v104, v2
	v_mov_b32_e32 v105, v2
	v_mov_b32_e32 v130, v2
	v_mov_b32_e32 v131, v2
	v_mov_b32_e32 v132, v2
	v_mov_b32_e32 v133, v2
	v_mov_b32_e32 v134, v2
	v_mov_b32_e32 v135, v2
	v_mov_b32_e32 v136, v2
	v_mov_b32_e32 v137, v2
	v_mov_b32_e32 v74, v2
	v_mov_b32_e32 v75, v2
	v_mov_b32_e32 v76, v2
	v_mov_b32_e32 v77, v2
	v_mov_b32_e32 v78, v2
	v_mov_b32_e32 v79, v2
	v_mov_b32_e32 v80, v2
	v_mov_b32_e32 v81, v2
	v_mov_b32_e32 v90, v2
	v_mov_b32_e32 v91, v2
	v_mov_b32_e32 v92, v2
	v_mov_b32_e32 v93, v2
	v_mov_b32_e32 v94, v2
	v_mov_b32_e32 v95, v2
	v_mov_b32_e32 v96, v2
	v_mov_b32_e32 v97, v2
	v_mov_b32_e32 v114, v2
	v_mov_b32_e32 v115, v2
	v_mov_b32_e32 v116, v2
	v_mov_b32_e32 v117, v2
	v_mov_b32_e32 v118, v2
	v_mov_b32_e32 v119, v2
	v_mov_b32_e32 v120, v2
	v_mov_b32_e32 v121, v2
	v_mov_b32_e32 v138, v2
	v_mov_b32_e32 v139, v2
	v_mov_b32_e32 v140, v2
	v_mov_b32_e32 v141, v2
	v_mov_b32_e32 v142, v2
	v_mov_b32_e32 v143, v2
	v_mov_b32_e32 v144, v2
	v_mov_b32_e32 v145, v2
	v_mov_b32_e32 v62, v2
	v_mov_b32_e32 v63, v2
	v_mov_b32_e32 v64, v2
	v_mov_b32_e32 v65, v2
	v_mov_b32_e32 v58, v2
	v_mov_b32_e32 v59, v2
	v_mov_b32_e32 v60, v2
	v_mov_b32_e32 v61, v2
	v_mov_b32_e32 v46, v2
	v_mov_b32_e32 v47, v2
	v_mov_b32_e32 v48, v2
	v_mov_b32_e32 v49, v2
	v_mov_b32_e32 v42, v2
	v_mov_b32_e32 v43, v2
	v_mov_b32_e32 v44, v2
	v_mov_b32_e32 v45, v2
	v_mov_b32_e32 v30, v2
	v_mov_b32_e32 v31, v2
	v_mov_b32_e32 v32, v2
	v_mov_b32_e32 v33, v2
	v_mov_b32_e32 v26, v2
	v_mov_b32_e32 v27, v2
	v_mov_b32_e32 v28, v2
	v_mov_b32_e32 v29, v2
	v_mov_b32_e32 v14, v2
	v_mov_b32_e32 v15, v2
	v_mov_b32_e32 v16, v2
	v_mov_b32_e32 v17, v2
	v_mov_b32_e32 v10, v2
	v_mov_b32_e32 v11, v2
	v_mov_b32_e32 v12, v2
	v_mov_b32_e32 v13, v2
	.p2align	6

.LBB0_2072:
	s_add_u32 s5, s26, 0x100
	s_addc_u32 s17, s27, 0
	s_add_u32 s18, s22, 0x100
	s_addc_u32 s19, s23, 0
	s_add_u32 s22, s22, 0x80
	s_addc_u32 s23, s23, 0
	s_mov_b32 s21, -2
	.p2align	6
